# r1 + grid barrier: each workgroup's acquire-side L1 invalidate (buffer_inv sc1) is issued at barrier entry beside its arrival atomic instead of after the release is observed (the XCD leader keeps its
# speedup vs baseline: 1.0150x; 1.0150x over previous
.LBB0_764:
	v_readlane_b32 s4, v243, 61
	v_readlane_b32 s5, v243, 62
	v_cvt_f32_u32_e32 v1, v4
	v_sub_u32_e32 v6, 0, v4
	v_rcp_iflag_f32_e32 v1, v1
	s_nop 1
	buffer_inv sc1
	global_atomic_add v5, v3, v216, s[4:5] sc0
	v_mul_f32_e32 v1, 0x4f7ffffe, v1
	v_cvt_u32_f32_e32 v1, v1
	v_mul_lo_u32 v6, v6, v1
	v_mul_hi_u32 v6, v1, v6
	v_add_u32_e32 v1, v1, v6
	s_waitcnt vmcnt(0)
	v_mul_hi_u32 v1, v5, v1
	v_mul_lo_u32 v6, v1, v4
	v_sub_u32_e32 v6, v5, v6
	v_add_u32_e32 v7, 1, v1
	v_cmp_ge_u32_e32 vcc, v6, v4
	v_add_u32_e32 v5, 1, v5
	s_nop 0
	v_cndmask_b32_e32 v1, v1, v7, vcc
	v_sub_u32_e32 v7, v6, v4
	v_cndmask_b32_e32 v6, v6, v7, vcc
	v_add_u32_e32 v7, 1, v1
	v_cmp_ge_u32_e32 vcc, v6, v4
	s_nop 1
	v_cndmask_b32_e32 v1, v1, v7, vcc
	v_mul_lo_u32 v6, v4, v1
	v_add_u32_e32 v4, v6, v4
	v_cmp_ne_u32_e32 vcc, v5, v4
	s_and_saveexec_b64 s[4:5], vcc
	s_xor_b64 s[4:5], exec, s[4:5]
	s_cbranch_execz .LBB0_778
	s_waitcnt lgkmcnt(0)
	global_load_dword v2, v3, s[82:83] sc1
	s_waitcnt vmcnt(0)
	v_cmp_eq_u32_e32 vcc, v2, v1
	s_and_saveexec_b64 s[6:7], vcc
	s_cbranch_execz .LBB0_777
	s_mov_b32 s19, 1
	s_mov_b64 s[8:9], 0
	s_branch .LBB0_768

.LBB0_777:
	s_or_b64 exec, exec, s[6:7]
	s_waitcnt vmcnt(0)
	s_nop 0
	s_waitcnt vmcnt(0)

.LBB0_2938:
	v_readlane_b32 s4, v243, 61
	v_readlane_b32 s5, v243, 62
	v_cvt_f32_u32_e32 v1, v4
	v_sub_u32_e32 v6, 0, v4
	v_rcp_iflag_f32_e32 v1, v1
	s_nop 1
	buffer_inv sc1
	global_atomic_add v5, v3, v216, s[4:5] sc0
	v_mul_f32_e32 v1, 0x4f7ffffe, v1
	v_cvt_u32_f32_e32 v1, v1
	v_mul_lo_u32 v6, v6, v1
	v_mul_hi_u32 v6, v1, v6
	v_add_u32_e32 v1, v1, v6
	s_waitcnt vmcnt(0)
	v_mul_hi_u32 v1, v5, v1
	v_mul_lo_u32 v6, v1, v4
	v_sub_u32_e32 v6, v5, v6
	v_add_u32_e32 v7, 1, v1
	v_cmp_ge_u32_e32 vcc, v6, v4
	v_add_u32_e32 v5, 1, v5
	s_nop 0
	v_cndmask_b32_e32 v1, v1, v7, vcc
	v_sub_u32_e32 v7, v6, v4
	v_cndmask_b32_e32 v6, v6, v7, vcc
	v_add_u32_e32 v7, 1, v1
	v_cmp_ge_u32_e32 vcc, v6, v4
	s_nop 1
	v_cndmask_b32_e32 v1, v1, v7, vcc
	v_mul_lo_u32 v6, v4, v1
	v_add_u32_e32 v4, v6, v4
	v_cmp_ne_u32_e32 vcc, v5, v4
	s_and_saveexec_b64 s[4:5], vcc
	s_xor_b64 s[4:5], exec, s[4:5]
	s_cbranch_execz .LBB0_2952
	s_waitcnt lgkmcnt(0)
	global_load_dword v2, v3, s[82:83] sc1
	s_waitcnt vmcnt(0)
	v_cmp_eq_u32_e32 vcc, v2, v1
	s_and_saveexec_b64 s[6:7], vcc
	s_cbranch_execz .LBB0_2951
	s_mov_b32 s18, 1
	s_mov_b64 s[8:9], 0
	s_branch .LBB0_2942
